# static s_setprio 2 for the GDN scan's compute waves (each shares a SIMD with a loader / store wave)
# baseline (speedup 1.0000x reference)
.LBB0_442:
	s_and_b64 vcc, exec, s[0:1]
	s_cbranch_vccz .LBB0_456
	s_and_b32 s6, s30, 7
	s_ashr_i32 s7, s30, 1
	s_bfe_u32 s8, s30, 0x10003
	s_cmp_lg_u32 s80, 7
	v_lshlrev_b32_e32 v190, 4, v237
	v_lshlrev_b32_e32 v191, 3, v236
	s_mov_b64 s[0:1], -1
	s_cbranch_scc0 .LBB0_453
	s_and_b32 s0, s7, 0x3fffff8
	s_or_b32 s1, s0, s6
	s_lshl_b32 s0, s1, 6
	s_mul_i32 s1, s1, 0x480000
	s_mul_hi_i32 s2, s0, 0x12000
	s_add_u32 s4, s40, s1
	s_addc_u32 s5, s41, s2
	v_readlane_b32 s1, v253, 9
	s_cmpk_lt_u32 s1, 0x100
	s_mov_b64 s[2:3], -1
	s_cbranch_scc0 .LBB0_448
	s_setprio 2
	s_ashr_i32 s1, s0, 31
	v_readlane_b32 s2, v253, 9
	s_lshr_b32 s15, s2, 7
	s_lshl_b64 s[0:1], s[0:1], 2
	s_add_u32 s0, s88, s0
	s_addc_u32 s1, s89, s1
	v_lshlrev_b32_e32 v104, 2, v237
	v_mov_b32_e32 v105, 0
	v_lshl_add_u64 v[0:1], s[0:1], 0, v[104:105]
	s_lshl_b32 s0, s15, 13
	s_add_i32 s0, s0, 0
	s_bfe_u32 s19, s2, 0x10006
	s_add_i32 s20, s0, 0x1e000
	s_lshl_b32 s0, s8, 13
	s_lshl_b32 s13, s15, 12
	s_lshl_b32 s16, s19, 2
	s_lshl_b32 s22, s19, 12
	s_add_i32 s9, s13, s0
	s_mov_b32 s2, 0x500000
	s_add_u32 s0, s4, s9
	v_add_co_u32_e32 v0, vcc, s2, v0
	s_addc_u32 s1, s5, 0
	s_lshl_b32 s10, s19, 11
	v_addc_co_u32_e32 v1, vcc, 0, v1, vcc
	v_lshl_or_b32 v104, v237, 5, s10
	global_load_dword v6, v[0:1], off sc1
	v_lshl_add_u64 v[0:1], s[0:1], 0, v[104:105]
	s_mov_b64 s[0:1], 0xe000
	s_waitcnt vmcnt(1)
	v_lshl_add_u64 v[2:3], v[0:1], 0, s[0:1]
	s_mov_b32 s0, 0xe000
	v_add_co_u32_e32 v4, vcc, s0, v0
	s_lshl_b32 s1, s19, 1
	s_nop 0
	v_addc_co_u32_e32 v5, vcc, 0, v1, vcc
	global_load_dwordx4 v[52:55], v[4:5], off
	global_load_dwordx4 v[48:51], v[2:3], off offset:16
	s_mov_b64 s[2:3], 0x20000
	s_xor_b32 s1, s1, 2
	v_lshl_add_u64 v[2:3], v[0:1], 0, s[2:3]
	s_lshl_b32 s23, s1, 11
	s_or_b32 s1, s1, s16
	s_mul_i32 s2, s19, 0x300
	v_or_b32_e32 v5, s2, v237
	v_lshl_or_b32 v107, s1, 11, v190
	s_add_i32 s1, 0, 0x1c000
	s_sub_i32 s2, s13, s10
	s_add_i32 s12, s1, s13
	s_add_i32 s13, s1, s2
	s_add_i32 s1, s22, 0
	s_add_i32 s25, s1, 0x22000
	s_or_b32 s1, s16, 2
	v_and_b32_e32 v8, 0x100, v191
	s_or_b32 s2, s1, s19
	s_mov_b32 s0, 0
	s_mul_i32 s14, s19, 0x1800
	v_lshl_add_u32 v8, s15, 5, v8
	s_mul_i32 s15, s19, 0x2800
	s_lshl_b32 s17, s2, 11
	s_sub_i32 s1, s1, s19
	s_mulk_i32 s19, 0x280
	s_add_i32 s2, 0, 0x1a000
	s_add_i32 s24, 0, 0x16000
	s_lshl_b32 s1, s1, 11
	v_or_b32_e32 v9, s19, v237
	v_add_u32_e32 v112, s2, v190
	s_mov_b32 s2, s0
	s_mov_b32 s3, s0
	v_add_u32_e32 v4, s20, v190
	v_lshlrev_b32_e32 v106, 4, v5
	v_and_or_b32 v8, v236, 31, v8
	s_add_i32 s18, s1, 0
	v_lshlrev_b32_e32 v110, 4, v9
	v_or_b32_e32 v111, s17, v190
	s_add_i32 s21, s24, s1
	s_mov_b32 s1, s0
	v_mov_b64_e32 v[14:15], s[2:3]
	s_mov_b32 s11, 1
	v_or_b32_e32 v5, 0x800, v106
	v_or_b32_e32 v7, 0x800, v107
	s_add_i32 s12, s12, s10
	v_add_u32_e32 v108, 0, v190
	v_add_u32_e32 v109, s24, v190
	v_lshlrev_b32_e32 v8, 1, v8
	s_add_i32 s16, s14, 0
	v_or_b32_e32 v9, 0x400, v110
	v_or_b32_e32 v10, 0x400, v111
	s_add_i32 s19, s20, s22
	s_add_i32 s20, s24, s14
	v_add_u32_e32 v11, s22, v4
	v_mov_b64_e32 v[12:13], s[0:1]
	ds_write_b128 v11, v[12:15]
	ds_write_b128 v11, v[12:15] offset:1024
	ds_write_b128 v11, v[12:15] offset:2048
	ds_write_b128 v11, v[12:15] offset:3072
	s_waitcnt vmcnt(2)
	v_mul_f32_e32 v6, 0x3fb8aa3b, v6
	v_exp_f32_e32 v113, v6
	s_mov_b32 s0, 0x20000
	v_add_co_u32_e32 v0, vcc, s0, v0
	s_nop 1
	v_addc_co_u32_e32 v1, vcc, 0, v1, vcc
	global_load_dwordx4 v[60:63], v[0:1], off
	global_load_dwordx4 v[56:59], v[2:3], off offset:16
	s_waitcnt lgkmcnt(0)
	s_barrier
	v_add_u32_e32 v115, s23, v4
	s_add_i32 s23, 0, 0x12000
	s_mov_b64 s[0:1], 0x32000
	s_mov_b32 s3, 0x32000
	s_mov_b32 s22, 0x5040100
	v_add_u32_e32 v114, s25, v8
	v_add_u32_e32 v116, 0, v106
	v_add_u32_e32 v117, s23, v5
	v_add_u32_e32 v118, s23, v7
	v_add_u32_e32 v119, s24, v9
	v_add_u32_e32 v120, s24, v10
	v_mov_b32_e32 v0, v105
	v_mov_b32_e32 v1, v105
	v_mov_b32_e32 v2, v105
	v_mov_b32_e32 v3, v105
	v_mov_b32_e32 v4, v105
	v_mov_b32_e32 v5, v105
	v_mov_b32_e32 v6, v105
	v_mov_b32_e32 v7, v105
	v_mov_b32_e32 v8, v105
	v_mov_b32_e32 v9, v105
	v_mov_b32_e32 v10, v105
	v_mov_b32_e32 v11, v105
	v_mov_b32_e32 v12, v105
	v_mov_b32_e32 v13, v105
	v_mov_b32_e32 v14, v105
	v_mov_b32_e32 v15, v105
	v_mov_b32_e32 v16, v105
	v_mov_b32_e32 v17, v105
	v_mov_b32_e32 v18, v105
	v_mov_b32_e32 v19, v105
	v_mov_b32_e32 v20, v105
	v_mov_b32_e32 v21, v105
	v_mov_b32_e32 v22, v105
	v_mov_b32_e32 v23, v105
	v_mov_b32_e32 v24, v105
	v_mov_b32_e32 v25, v105
	v_mov_b32_e32 v26, v105
	v_mov_b32_e32 v27, v105
	v_mov_b32_e32 v28, v105
	v_mov_b32_e32 v29, v105
	v_mov_b32_e32 v30, v105
	v_mov_b32_e32 v31, v105
.LBB0_446:
	ds_read_b128 v[32:35], v116
	ds_read_b128 v[68:71], v116 offset:1024
	v_cvt_pk_bf16_f32 v64, v0, v1
	v_cvt_pk_bf16_f32 v65, v2, v3
	v_cvt_pk_bf16_f32 v66, v4, v5
	v_cvt_pk_bf16_f32 v67, v6, v7
	v_add_u32_e32 v96, 0, v107
	ds_read_b128 v[72:75], v96
	ds_read_b128 v[76:79], v115
	ds_read_b128 v[80:83], v115 offset:1024
	ds_read_b128 v[84:87], v96 offset:1024
	s_add_i32 s24, s11, -1
	s_waitcnt lgkmcnt(5)
	v_mfma_f32_32x32x16_bf16 v[32:47], v[32:35], v[64:67], 0
	ds_read_b128 v[88:91], v116 offset:3072
	s_waitcnt lgkmcnt(3)
	v_mfma_f32_32x32x16_bf16 v[32:47], v[72:75], v[76:79], v[32:47]
	v_cvt_pk_bf16_f32 v72, v8, v9
	v_cvt_pk_bf16_f32 v73, v10, v11
	v_cvt_pk_bf16_f32 v74, v12, v13
	v_cvt_pk_bf16_f32 v75, v14, v15
	s_nop 1
	v_mfma_f32_32x32x16_bf16 v[32:47], v[68:71], v[72:75], v[32:47]
	ds_read_b128 v[68:71], v116 offset:2048
	s_waitcnt lgkmcnt(2)
	v_mfma_f32_32x32x16_bf16 v[32:47], v[84:87], v[80:83], v[32:47]
	v_cvt_pk_bf16_f32 v84, v16, v17
	v_cvt_pk_bf16_f32 v85, v18, v19
	v_cvt_pk_bf16_f32 v86, v20, v21
	v_cvt_pk_bf16_f32 v87, v22, v23
	s_waitcnt lgkmcnt(0)
	s_nop 0
	v_mfma_f32_32x32x16_bf16 v[32:47], v[68:71], v[84:87], v[32:47]
	ds_read_b128 v[68:71], v96 offset:2048
	ds_read_b128 v[92:95], v115 offset:2048
	ds_read_b128 v[98:101], v115 offset:3072
	ds_read_b128 v[122:125], v96 offset:3072
	s_waitcnt lgkmcnt(2)
	v_mfma_f32_32x32x16_bf16 v[32:47], v[68:71], v[92:95], v[32:47]
	v_cvt_pk_bf16_f32 v68, v24, v25
	v_cvt_pk_bf16_f32 v69, v26, v27
	v_cvt_pk_bf16_f32 v70, v28, v29
	v_cvt_pk_bf16_f32 v71, v30, v31
	s_nop 1
	v_mfma_f32_32x32x16_bf16 v[32:47], v[88:91], v[68:71], v[32:47]
	s_waitcnt lgkmcnt(0)
	v_mfma_f32_32x32x16_bf16 v[32:47], v[122:125], v[98:101], v[32:47]
	s_waitcnt vmcnt(3)
	v_lshlrev_b32_e32 v88, 16, v52
	s_nop 9
	v_sub_f32_e32 v88, v88, v32
	v_and_b32_e32 v32, 0xffff0000, v52
	v_sub_f32_e32 v89, v32, v33
	v_lshlrev_b32_e32 v32, 16, v53
	v_sub_f32_e32 v90, v32, v34
	v_and_b32_e32 v32, 0xffff0000, v53
	v_sub_f32_e32 v91, v32, v35
	v_lshlrev_b32_e32 v32, 16, v54
	v_sub_f32_e32 v97, v32, v36
	v_and_b32_e32 v32, 0xffff0000, v54
	v_sub_f32_e32 v102, v32, v37
	v_lshlrev_b32_e32 v32, 16, v55
	v_sub_f32_e32 v103, v32, v38
	v_and_b32_e32 v32, 0xffff0000, v55
	v_sub_f32_e32 v121, v32, v39
	s_waitcnt vmcnt(2)
	v_lshlrev_b32_e32 v32, 16, v48
	v_sub_f32_e32 v122, v32, v40
	v_and_b32_e32 v32, 0xffff0000, v48
	v_sub_f32_e32 v123, v32, v41
	v_lshlrev_b32_e32 v32, 16, v49
	v_sub_f32_e32 v124, v32, v42
	v_and_b32_e32 v32, 0xffff0000, v49
	v_sub_f32_e32 v125, v32, v43
	v_lshlrev_b32_e32 v32, 16, v50
	v_sub_f32_e32 v126, v32, v44
	v_and_b32_e32 v32, 0xffff0000, v50
	v_sub_f32_e32 v127, v32, v45
	v_lshlrev_b32_e32 v32, 16, v51
	v_sub_f32_e32 v128, v32, v46
	v_and_b32_e32 v32, 0xffff0000, v51
	v_sub_f32_e32 v129, v32, v47
	ds_read_b128 v[32:35], v116 offset:16384
	ds_read_b128 v[48:51], v116 offset:17408
	s_min_u32 s2, s24, 61
	s_mul_i32 s2, s2, 0x12000
	s_add_u32 s2, s4, s2
	s_waitcnt lgkmcnt(1)
	v_mfma_f32_32x32x16_bf16 v[32:47], v[32:35], v[64:67], 0
	ds_read_b128 v[52:55], v96 offset:16384
	ds_read_b128 v[64:67], v96 offset:17408
	s_addc_u32 s25, s5, 0
	s_add_u32 s26, s2, s9
	s_addc_u32 s27, s25, 0
	v_cvt_pk_bf16_f32 v130, v88, s0
	v_cvt_pk_bf16_f32 v131, v89, s0
	v_cvt_pk_bf16_f32 v132, v123, s0
	s_waitcnt lgkmcnt(1)
	v_mfma_f32_32x32x16_bf16 v[32:47], v[52:55], v[76:79], v[32:47]
	v_cvt_pk_bf16_f32 v52, v88, v89
	v_cvt_pk_bf16_f32 v88, v90, s0
	v_cvt_pk_bf16_f32 v53, v90, v91
	v_cvt_pk_bf16_f32 v90, v97, s0
	v_cvt_pk_bf16_f32 v54, v97, v102
	v_cvt_pk_bf16_f32 v97, v103, s0
	v_cvt_pk_bf16_f32 v55, v103, v121
	v_mfma_f32_32x32x16_bf16 v[32:47], v[48:51], v[72:75], v[32:47]
	ds_read_b128 v[48:51], v116 offset:18432
	ds_read_b128 v[72:75], v96 offset:18432
	ds_read_b128 v[76:79], v116 offset:19456
	v_cvt_pk_bf16_f32 v103, v122, s0
	v_cvt_pk_bf16_f32 v89, v91, s0
	v_cvt_pk_bf16_f32 v91, v102, s0
	v_cvt_pk_bf16_f32 v102, v121, s0
	v_add_u32_e32 v121, s13, v190
	s_waitcnt lgkmcnt(3)
	v_mfma_f32_32x32x16_bf16 v[32:47], v[64:67], v[80:83], v[32:47]
	ds_read_b128 v[80:83], v96 offset:19456
	v_cvt_pk_bf16_f32 v64, v122, v123
	v_cvt_pk_bf16_f32 v65, v124, v125
	v_cvt_pk_bf16_f32 v66, v126, v127
	v_cvt_pk_bf16_f32 v67, v128, v129
	v_add_u32_e32 v122, s12, v190
	ds_write_b128 v122, v[52:55]
	s_waitcnt lgkmcnt(4)
	v_mfma_f32_32x32x16_bf16 v[32:47], v[48:51], v[84:87], v[32:47]
	v_lshl_add_u64 v[48:49], s[26:27], 0, v[104:105]
	v_lshl_add_u64 v[50:51], v[48:49], 0, s[0:1]
	v_add_co_u32_e32 v48, vcc, s3, v48
	ds_write_b128 v122, v[64:67] offset:1024
	s_nop 0
	v_addc_co_u32_e32 v49, vcc, 0, v49, vcc
	s_waitcnt lgkmcnt(4)
	v_mfma_f32_32x32x16_bf16 v[32:47], v[72:75], v[92:95], v[32:47]
	v_add_u32_e32 v84, s14, v108
	global_load_dwordx4 v[52:55], v[48:49], off
	s_nop 0
	global_load_dwordx4 v[48:51], v[50:51], off offset:16
	s_waitcnt lgkmcnt(0)
	s_barrier
	ds_read_b128 v[64:67], v84 offset:49152
	v_add_u32_e32 v85, s10, v108
	s_waitcnt lgkmcnt(4)
	v_mfma_f32_32x32x16_bf16 v[32:47], v[76:79], v[68:71], v[32:47]
	v_perm_b32 v70, v91, v90, s22
	v_perm_b32 v69, v89, v88, s22
	v_perm_b32 v68, v131, v130, s22
	v_perm_b32 v71, v102, v97, s22
	ds_read_b128 v[72:75], v85 offset:51200
	ds_read_b128 v[76:79], v84 offset:50176
	v_cvt_pk_bf16_f32 v88, v124, s0
	v_cvt_pk_bf16_f32 v89, v125, s0
	s_waitcnt lgkmcnt(5)
	v_mfma_f32_32x32x16_bf16 v[32:47], v[80:83], v[98:101], v[32:47]
	v_cvt_pk_bf16_f32 v90, v126, s0
	v_cvt_pk_bf16_f32 v91, v129, s0
	v_readlane_b32 s2, v113, s24
	v_add_u32_e32 v123, s19, v190
	s_nop 0
	v_mul_f32_e64 v14, v14, s2
	v_mul_f32_e64 v15, v15, s2
	v_pk_mul_f32 v[12:13], v[12:13], s[2:3] op_sel_hi:[1,0]
	s_waitcnt lgkmcnt(2)
	v_mfma_f32_32x32x16_bf16 v[32:47], v[64:67], v[68:71], v[32:47]
	ds_read_b128 v[64:67], v121 offset:2048
	ds_read_b128 v[80:83], v121 offset:3072
	ds_read_b128 v[84:87], v85 offset:52224
	v_mul_f32_e64 v10, v10, s2
	v_mul_f32_e64 v11, v11, s2
	v_pk_mul_f32 v[8:9], v[8:9], s[2:3] op_sel_hi:[1,0]
	v_pk_mul_f32 v[6:7], v[6:7], s[2:3] op_sel_hi:[1,0]
	v_pk_mul_f32 v[4:5], v[4:5], s[2:3] op_sel_hi:[1,0]
	v_pk_mul_f32 v[2:3], v[2:3], s[2:3] op_sel_hi:[1,0]
	s_waitcnt lgkmcnt(2)
	v_mfma_f32_32x32x16_bf16 v[32:47], v[72:75], v[64:67], v[32:47]
	v_cvt_pk_bf16_f32 v72, v127, s0
	v_cvt_pk_bf16_f32 v75, v128, s0
	v_perm_b32 v74, v72, v90, s22
	v_perm_b32 v73, v89, v88, s22
	v_perm_b32 v72, v132, v103, s22
	v_perm_b32 v75, v91, v75, s22
	v_add_u32_e32 v88, s16, v190
	v_pk_mul_f32 v[0:1], v[0:1], s[2:3] op_sel_hi:[1,0]
	v_mfma_f32_32x32x16_bf16 v[32:47], v[76:79], v[72:75], v[32:47]
	v_add_u32_e32 v76, s15, v108
	ds_read_b128 v[76:79], v76 offset:32768
	v_mul_f32_e64 v30, v30, s2
	v_mul_f32_e64 v31, v31, s2
	v_mul_f32_e64 v28, v28, s2
	v_mul_f32_e64 v29, v29, s2
	v_pk_mul_f32 v[26:27], v[26:27], s[2:3] op_sel_hi:[1,0]
	v_pk_mul_f32 v[24:25], v[24:25], s[2:3] op_sel_hi:[1,0]
	v_pk_mul_f32 v[22:23], v[22:23], s[2:3] op_sel_hi:[1,0]
	s_waitcnt lgkmcnt(1)
	v_mfma_f32_32x32x16_bf16 v[32:47], v[84:87], v[80:83], v[32:47]
	ds_read_b128 v[84:87], v88 offset:34816
	v_mul_f32_e64 v20, v20, s2
	v_mul_f32_e64 v21, v21, s2
	v_mul_f32_e64 v18, v18, s2
	v_mul_f32_e64 v19, v19, s2
	v_pk_mul_f32 v[16:17], v[16:17], s[2:3] op_sel_hi:[1,0]
	s_waitcnt lgkmcnt(1)
	v_mfma_f32_32x32x16_bf16 v[0:15], v[76:79], v[68:71], v[0:15]
	v_add_u32_e32 v76, s17, v108
	ds_read_b128 v[76:79], v76 offset:32768
	s_nop 1
	v_cvt_pk_bf16_f32 v32, v32, s0
	ds_write_b16 v114, v32
	v_add_u32_e32 v32, s18, v190
	v_cvt_pk_bf16_f32 v33, v33, s0
	s_waitcnt lgkmcnt(1)
	v_mfma_f32_32x32x16_bf16 v[16:31], v[76:79], v[68:71], v[16:31]
	v_mfma_f32_32x32x16_bf16 v[0:15], v[84:87], v[64:67], v[0:15]
	ds_read_b128 v[84:87], v32 offset:34816
	ds_read_b128 v[88:91], v88 offset:35840
	ds_write_b16 v114, v33 offset:128
	v_cvt_pk_bf16_f32 v33, v34, s0
	ds_write_b16 v114, v33 offset:256
	v_add_u32_e32 v33, 0, v110
	ds_read_b128 v[68:71], v33 offset:33792
	ds_read_b128 v[76:79], v32 offset:35840
	v_cvt_pk_bf16_f32 v32, v35, s0
	ds_write_b16 v114, v32 offset:384
	v_cvt_pk_bf16_f32 v32, v36, s0
	ds_write_b16 v114, v32 offset:1024
	v_add_u32_e32 v32, 0, v111
	ds_read_b128 v[32:35], v32 offset:33792
	s_waitcnt lgkmcnt(8)
	v_mfma_f32_32x32x16_bf16 v[16:31], v[84:87], v[64:67], v[16:31]
	v_cvt_pk_bf16_f32 v36, v37, s0
	ds_write_b16 v114, v36 offset:1152
	v_cvt_pk_bf16_f32 v36, v38, s0
	ds_write_b16 v114, v36 offset:1280
	v_cvt_pk_bf16_f32 v36, v39, s0
	ds_write_b16 v114, v36 offset:1408
	v_cvt_pk_bf16_f32 v36, v40, s0
	s_waitcnt lgkmcnt(7)
	v_mfma_f32_32x32x16_bf16 v[0:15], v[68:71], v[72:75], v[0:15]
	ds_write_b16 v114, v36 offset:2048
	v_cvt_pk_bf16_f32 v36, v41, s0
	ds_write_b16 v114, v36 offset:2176
	v_cvt_pk_bf16_f32 v36, v42, s0
	ds_write_b16 v114, v36 offset:2304
	v_cvt_pk_bf16_f32 v36, v43, s0
	ds_write_b16 v114, v36 offset:2432
	s_waitcnt lgkmcnt(7)
	v_mfma_f32_32x32x16_bf16 v[16:31], v[32:35], v[72:75], v[16:31]
	v_cvt_pk_bf16_f32 v32, v45, s0
	ds_write_b16 v114, v32 offset:3200
	v_cvt_pk_bf16_f32 v32, v46, s0
	v_cvt_pk_bf16_f32 v36, v44, s0
	ds_write_b16 v114, v32 offset:3328
	v_cvt_pk_bf16_f32 v32, v47, s0
	ds_write_b16 v114, v36 offset:3072
	v_mfma_f32_32x32x16_bf16 v[0:15], v[88:91], v[80:83], v[0:15]
	ds_write_b16 v114, v32 offset:3456
	v_mfma_f32_32x32x16_bf16 v[16:31], v[76:79], v[80:83], v[16:31]
	s_nop 9
	v_cvt_pk_bf16_f32 v76, v0, v1
	v_cvt_pk_bf16_f32 v77, v2, v3
	v_cvt_pk_bf16_f32 v78, v4, v5
	v_cvt_pk_bf16_f32 v79, v6, v7
	v_cvt_pk_bf16_f32 v72, v8, v9
	v_cvt_pk_bf16_f32 v73, v10, v11
	v_cvt_pk_bf16_f32 v74, v12, v13
	v_cvt_pk_bf16_f32 v75, v14, v15
	v_cvt_pk_bf16_f32 v64, v16, v17
	v_cvt_pk_bf16_f32 v65, v18, v19
	v_cvt_pk_bf16_f32 v66, v20, v21
	v_cvt_pk_bf16_f32 v67, v22, v23
	v_cvt_pk_bf16_f32 v68, v24, v25
	v_cvt_pk_bf16_f32 v69, v26, v27
	v_cvt_pk_bf16_f32 v70, v28, v29
	v_cvt_pk_bf16_f32 v71, v30, v31
	ds_write_b128 v123, v[76:79]
	ds_write_b128 v123, v[72:75] offset:1024
	ds_write_b128 v123, v[64:67] offset:2048
	ds_write_b128 v123, v[68:71] offset:3072
	s_waitcnt lgkmcnt(0)
	s_barrier
	ds_read_b128 v[32:35], v116 offset:57344
	ds_read_b128 v[84:87], v116 offset:58368
	s_waitcnt lgkmcnt(1)
	v_mfma_f32_32x32x16_bf16 v[32:47], v[32:35], v[76:79], 0
	ds_read_b128 v[88:91], v96 offset:57344
	ds_read_b128 v[92:95], v115
	ds_read_b128 v[80:83], v115 offset:1024
	ds_read_b128 v[98:101], v96 offset:58368
	s_waitcnt lgkmcnt(2)
	v_mfma_f32_32x32x16_bf16 v[32:47], v[88:91], v[92:95], v[32:47]
	v_mfma_f32_32x32x16_bf16 v[32:47], v[84:87], v[72:75], v[32:47]
	s_waitcnt lgkmcnt(0)
	v_mfma_f32_32x32x16_bf16 v[32:47], v[98:101], v[80:83], v[32:47]
	ds_read_b128 v[84:87], v116 offset:59392
	ds_read_b128 v[98:101], v116 offset:60416
	s_waitcnt lgkmcnt(1)
	v_mfma_f32_32x32x16_bf16 v[32:47], v[84:87], v[64:67], v[32:47]
	ds_read_b128 v[124:127], v96 offset:59392
	ds_read_b128 v[88:91], v115 offset:2048
	ds_read_b128 v[84:87], v115 offset:3072
	ds_read_b128 v[128:131], v96 offset:60416
	s_waitcnt lgkmcnt(2)
	v_mfma_f32_32x32x16_bf16 v[32:47], v[124:127], v[88:91], v[32:47]
	v_mfma_f32_32x32x16_bf16 v[32:47], v[98:101], v[68:71], v[32:47]
	s_waitcnt lgkmcnt(0)
	v_mfma_f32_32x32x16_bf16 v[32:47], v[128:131], v[84:87], v[32:47]
	s_waitcnt vmcnt(3)
	v_lshlrev_b32_e32 v96, 16, v60
	v_and_b32_e32 v60, 0xffff0000, v60
	s_nop 8
	v_sub_f32_e32 v33, v60, v33
	v_lshlrev_b32_e32 v60, 16, v61
	v_sub_f32_e32 v34, v60, v34
	v_and_b32_e32 v60, 0xffff0000, v61
	v_sub_f32_e32 v35, v60, v35
	v_lshlrev_b32_e32 v60, 16, v62
	v_sub_f32_e32 v36, v60, v36
	v_and_b32_e32 v60, 0xffff0000, v62
	v_sub_f32_e32 v37, v60, v37
	v_lshlrev_b32_e32 v60, 16, v63
	v_sub_f32_e32 v38, v60, v38
	v_and_b32_e32 v60, 0xffff0000, v63
	v_sub_f32_e32 v39, v60, v39
	s_waitcnt vmcnt(2)
	v_lshlrev_b32_e32 v60, 16, v56
	v_sub_f32_e32 v148, v60, v40
	v_and_b32_e32 v40, 0xffff0000, v56
	v_sub_f32_e32 v149, v40, v41
	v_lshlrev_b32_e32 v40, 16, v57
	v_sub_f32_e32 v150, v40, v42
	v_and_b32_e32 v40, 0xffff0000, v57
	v_sub_f32_e32 v151, v40, v43
	v_lshlrev_b32_e32 v40, 16, v58
	v_sub_f32_e32 v152, v40, v44
	v_and_b32_e32 v40, 0xffff0000, v58
	v_sub_f32_e32 v153, v40, v45
	v_lshlrev_b32_e32 v40, 16, v59
	v_sub_f32_e32 v154, v40, v46
	v_and_b32_e32 v40, 0xffff0000, v59
	v_sub_f32_e32 v32, v96, v32
	v_sub_f32_e32 v155, v40, v47
	v_cvt_pk_bf16_f32 v40, v32, s0
	v_cvt_pk_bf16_f32 v41, v33, s0
	v_cvt_pk_bf16_f32 v32, v32, v33
	v_cvt_pk_bf16_f32 v42, v34, s0
	v_cvt_pk_bf16_f32 v43, v35, s0
	v_cvt_pk_bf16_f32 v33, v34, v35
	v_cvt_pk_bf16_f32 v34, v36, v37
	v_cvt_pk_bf16_f32 v35, v38, v39
	v_cvt_pk_bf16_f32 v44, v36, s0
	v_cvt_pk_bf16_f32 v45, v37, s0
	v_cvt_pk_bf16_f32 v46, v38, s0
	v_cvt_pk_bf16_f32 v47, v39, s0
	v_cvt_pk_bf16_f32 v36, v148, v149
	v_cvt_pk_bf16_f32 v37, v150, v151
	v_cvt_pk_bf16_f32 v38, v152, v153
	v_cvt_pk_bf16_f32 v39, v154, v155
	v_add_u32_e32 v56, s23, v106
	ds_read_b128 v[96:99], v117
	ds_read_b128 v[100:103], v117 offset:1024
	ds_read_b128 v[124:127], v118
	ds_read_b128 v[128:131], v118 offset:1024
	ds_write_b128 v122, v[32:35]
	ds_write_b128 v122, v[36:39] offset:1024
	v_add_u32_e32 v57, s23, v107
	ds_read_b128 v[32:35], v56
	ds_read_b128 v[132:135], v56 offset:1024
	ds_read_b128 v[136:139], v57
	ds_read_b128 v[140:143], v57 offset:1024
	v_perm_b32 v146, v45, v44, s22
	v_perm_b32 v145, v43, v42, s22
	v_perm_b32 v144, v41, v40, s22
	v_perm_b32 v147, v47, v46, s22
	s_waitcnt lgkmcnt(3)
	v_mfma_f32_32x32x16_bf16 v[32:47], v[32:35], v[76:79], 0
	s_min_u32 s25, s11, 61
	v_readlane_b32 s2, v113, s11
	s_mul_i32 s25, s25, 0x12000
	v_add_u32_e32 v156, s15, v109
	v_mul_f32_e64 v14, v14, s2
	v_mul_f32_e64 v15, v15, s2
	v_pk_mul_f32 v[12:13], v[12:13], s[2:3] op_sel_hi:[1,0]
	v_pk_mul_f32 v[10:11], v[10:11], s[2:3] op_sel_hi:[1,0]
	s_waitcnt lgkmcnt(1)
	v_mfma_f32_32x32x16_bf16 v[32:47], v[136:139], v[92:95], v[32:47]
	v_mul_f32_e64 v8, v8, s2
	v_mul_f32_e64 v9, v9, s2
	v_mul_f32_e64 v6, v6, s2
	v_mul_f32_e64 v7, v7, s2
	v_mul_f32_e64 v4, v4, s2
	v_mul_f32_e64 v5, v5, s2
	v_pk_mul_f32 v[2:3], v[2:3], s[2:3] op_sel_hi:[1,0]
	v_pk_mul_f32 v[0:1], v[0:1], s[2:3] op_sel_hi:[1,0]
	v_pk_mul_f32 v[30:31], v[30:31], s[2:3] op_sel_hi:[1,0]
	v_pk_mul_f32 v[28:29], v[28:29], s[2:3] op_sel_hi:[1,0]
	v_pk_mul_f32 v[26:27], v[26:27], s[2:3] op_sel_hi:[1,0]
	v_pk_mul_f32 v[24:25], v[24:25], s[2:3] op_sel_hi:[1,0]
	v_pk_mul_f32 v[22:23], v[22:23], s[2:3] op_sel_hi:[1,0]
	v_pk_mul_f32 v[20:21], v[20:21], s[2:3] op_sel_hi:[1,0]
	v_pk_mul_f32 v[18:19], v[18:19], s[2:3] op_sel_hi:[1,0]
	v_pk_mul_f32 v[16:17], v[16:17], s[2:3] op_sel_hi:[1,0]
	s_add_u32 s2, s4, s25
	s_addc_u32 s25, s5, 0
	s_add_u32 s26, s2, s9
	v_mfma_f32_32x32x16_bf16 v[32:47], v[132:135], v[72:75], v[32:47]
	s_addc_u32 s27, s25, 0
	v_lshl_add_u64 v[56:57], s[26:27], 0, v[104:105]
	v_lshl_add_u64 v[58:59], v[56:57], 0, s[0:1]
	v_add_co_u32_e32 v56, vcc, s3, v56
	v_add_u32_e32 v157, s20, v190
	s_nop 0
	v_addc_co_u32_e32 v57, vcc, 0, v57, vcc
	global_load_dwordx4 v[60:63], v[56:57], off
	s_nop 0
	global_load_dwordx4 v[56:59], v[58:59], off offset:16
	s_waitcnt lgkmcnt(0)
	v_mfma_f32_32x32x16_bf16 v[32:47], v[140:143], v[80:83], v[32:47]
	s_waitcnt lgkmcnt(0)
	s_barrier
	ds_read_b128 v[76:79], v156
	ds_read_b128 v[92:95], v157 offset:2048
	v_add_u32_e32 v158, s17, v109
	v_add_u32_e32 v132, s21, v190
	v_cvt_pk_bf16_f32 v122, v148, s0
	v_mfma_f32_32x32x16_bf16 v[32:47], v[96:99], v[64:67], v[32:47]
	v_cvt_pk_bf16_f32 v148, v149, s0
	v_cvt_pk_bf16_f32 v149, v150, s0
	v_cvt_pk_bf16_f32 v150, v151, s0
	v_cvt_pk_bf16_f32 v151, v152, s0
	s_add_i32 s11, s11, 2
	s_cmp_gt_u32 s24, 61
	v_mfma_f32_32x32x16_bf16 v[32:47], v[124:127], v[88:91], v[32:47]
	v_mfma_f32_32x32x16_bf16 v[32:47], v[100:103], v[68:71], v[32:47]
	v_add_u32_e32 v68, s14, v112
	s_waitcnt lgkmcnt(1)
	v_mfma_f32_32x32x16_bf16 v[0:15], v[76:79], v[144:147], v[0:15]
	ds_read_b128 v[76:79], v158
	ds_read_b128 v[136:139], v157 offset:3072
	s_waitcnt lgkmcnt(1)
	v_mfma_f32_32x32x16_bf16 v[16:31], v[76:79], v[144:147], v[16:31]
	ds_read_b128 v[72:75], v121 offset:2048
	ds_read_b128 v[76:79], v121 offset:3072
	v_cvt_pk_bf16_f32 v121, v155, s0
	v_mfma_f32_32x32x16_bf16 v[32:47], v[128:131], v[84:87], v[32:47]
	s_waitcnt lgkmcnt(1)
	v_mfma_f32_32x32x16_bf16 v[0:15], v[92:95], v[72:75], v[0:15]
	ds_read_b128 v[92:95], v132 offset:2048
	ds_read_b128 v[132:135], v132 offset:3072
	ds_read_b128 v[80:83], v119
	ds_read_b128 v[140:143], v120
	ds_read_b128 v[64:67], v68
	ds_read_b128 v[68:71], v68 offset:1024
	s_waitcnt lgkmcnt(1)
	v_mfma_f32_32x32x16_bf16 v[32:47], v[64:67], v[144:147], v[32:47]
	v_mfma_f32_32x32x16_bf16 v[16:31], v[92:95], v[72:75], v[16:31]
	v_cvt_pk_bf16_f32 v92, v153, s0
	v_cvt_pk_bf16_f32 v95, v154, s0
	v_perm_b32 v94, v92, v151, s22
	v_perm_b32 v93, v150, v149, s22
	v_perm_b32 v92, v148, v122, s22
	v_perm_b32 v95, v121, v95, s22
	s_nop 1
	v_mfma_f32_32x32x16_bf16 v[0:15], v[80:83], v[92:95], v[0:15]
	v_add_u32_e32 v80, s10, v112
	ds_read_b128 v[64:67], v80 offset:2048
	ds_read_b128 v[80:83], v80 offset:3072
	s_waitcnt lgkmcnt(1)
	v_mfma_f32_32x32x16_bf16 v[32:47], v[64:67], v[72:75], v[32:47]
	v_mfma_f32_32x32x16_bf16 v[32:47], v[68:71], v[92:95], v[32:47]
	v_mfma_f32_32x32x16_bf16 v[16:31], v[140:143], v[92:95], v[16:31]
	s_waitcnt lgkmcnt(0)
	v_mfma_f32_32x32x16_bf16 v[32:47], v[80:83], v[76:79], v[32:47]
	v_mfma_f32_32x32x16_bf16 v[0:15], v[136:139], v[76:79], v[0:15]
	s_nop 10
	v_cvt_pk_bf16_f32 v32, v32, s0
	v_cvt_pk_bf16_f32 v33, v33, s0
	v_cvt_pk_bf16_f32 v34, v34, s0
	v_cvt_pk_bf16_f32 v35, v35, s0
	v_cvt_pk_bf16_f32 v36, v36, s0
	v_cvt_pk_bf16_f32 v37, v37, s0
	v_cvt_pk_bf16_f32 v38, v38, s0
	v_mfma_f32_32x32x16_bf16 v[16:31], v[132:135], v[76:79], v[16:31]
	v_cvt_pk_bf16_f32 v84, v0, v1
	v_cvt_pk_bf16_f32 v85, v2, v3
	v_cvt_pk_bf16_f32 v86, v4, v5
	v_cvt_pk_bf16_f32 v87, v6, v7
	v_cvt_pk_bf16_f32 v64, v8, v9
	v_cvt_pk_bf16_f32 v65, v10, v11
	v_cvt_pk_bf16_f32 v66, v12, v13
	v_cvt_pk_bf16_f32 v67, v14, v15
	s_nop 3
	v_cvt_pk_bf16_f32 v72, v16, v17
	v_cvt_pk_bf16_f32 v73, v18, v19
	v_cvt_pk_bf16_f32 v74, v20, v21
	v_cvt_pk_bf16_f32 v75, v22, v23
	v_cvt_pk_bf16_f32 v68, v24, v25
	v_cvt_pk_bf16_f32 v69, v26, v27
	v_cvt_pk_bf16_f32 v70, v28, v29
	v_cvt_pk_bf16_f32 v71, v30, v31
	v_cvt_pk_bf16_f32 v39, v39, s0
	v_cvt_pk_bf16_f32 v40, v40, s0
	v_cvt_pk_bf16_f32 v41, v41, s0
	v_cvt_pk_bf16_f32 v42, v42, s0
	v_cvt_pk_bf16_f32 v43, v43, s0
	v_cvt_pk_bf16_f32 v44, v44, s0
	v_cvt_pk_bf16_f32 v45, v45, s0
	v_cvt_pk_bf16_f32 v46, v46, s0
	v_cvt_pk_bf16_f32 v47, v47, s0
	ds_write_b16 v114, v32
	ds_write_b16 v114, v33 offset:128
	ds_write_b16 v114, v34 offset:256
	ds_write_b16 v114, v35 offset:384
	ds_write_b16 v114, v36 offset:1024
	ds_write_b16 v114, v37 offset:1152
	ds_write_b16 v114, v38 offset:1280
	ds_write_b16 v114, v39 offset:1408
	ds_write_b16 v114, v40 offset:2048
	ds_write_b16 v114, v41 offset:2176
	ds_write_b16 v114, v42 offset:2304
	ds_write_b16 v114, v43 offset:2432
	ds_write_b16 v114, v44 offset:3072
	ds_write_b16 v114, v45 offset:3200
	ds_write_b16 v114, v46 offset:3328
	ds_write_b16 v114, v47 offset:3456
	ds_write_b128 v123, v[84:87]
	ds_write_b128 v123, v[64:67] offset:1024
	ds_write_b128 v123, v[72:75] offset:2048
	ds_write_b128 v123, v[68:71] offset:3072
	s_waitcnt lgkmcnt(0)
	s_barrier
	s_cbranch_scc0 .LBB0_446
	s_setprio 0
	s_mov_b64 s[2:3], 0
